# adds 40 helper WGs in layer-0 proj GEMM phase (216 workers, 14 rounds) converting 22528 layer-0 MoE weight items deferred from the prologue
# baseline (speedup 1.0000x reference)
;     ...
;             const int itB = it + NGW;
;             if (itB < NIT) { dB = decode(NIT - 1 - itB); tr_load(dB, vB); }
.Lps_1:
	s_cmp_lt_i32 s44, 0x7e80
	s_cbranch_scc1 .Lpt_1
	s_cmp_ge_i32 s44, 0xd680
	s_cbranch_scc1 .Lpt_1
	s_add_i32 s44, s44, 0x5800

;     ...
;             const int itA = itB + NGW;
;             if (itA < NIT) { dA = decode(NIT - 1 - itA); tr_load(dA, vA); }
.Lps_2:
	s_cmp_lt_i32 s42, 0x7e80
	s_cbranch_scc1 .Lpt_2
	s_cmp_ge_i32 s42, 0xd680
	s_cbranch_scc1 .Lpt_2
	s_add_i32 s42, s42, 0x5800

;     ...
;         auto decode = [&](int it) -> TrDesc {
;             TrDesc d; d.zero = 0; d.rope = 0; d.f8 = 0;
;             const int l = it / C_L; int r = it % C_L;
;             const float* W; unsigned char* WT; int ldw, K, k0, n0, scol, esz = 2;
;             if (r < C_IN) { const int kb = r / 188, nb = r % 188; n0 = 64 * nb; k0 = 64 * kb; ldw = NIN; K = D; W = a.w_in + (size_t)l * D * NIN;
;                 if (n0 < 3072) { d.rope = 1; scol = (n0 >> 7) * 128 + 32 * ((n0 >> 6) & 1) + 64 * (q4 >> 3) + 4 * (q4 & 7); }
;                 else if (n0 < 7680) scol = n0 + 4 * q4;
;                 else if (n0 < 11776) scol = n0 + 16 + 4 * q4;
;                 else if (n0 == 11776) { scol = (q4 < 4) ? 7680 + 4 * q4 : 0; d.zero = (q4 < 4) ? 0 : 1; }
;                 else { scol = 0; d.zero = 1; }
;     ...
;                 d.f8 = 1; esz = 1; WT = ws + WS_WIN + (size_t)l * NP * D;
;     ...
;                 WT = ws + WS_WIN + (size_t)l * NP * D * 2;
;     ...
;             } else if ((r -= C_IN) < C_OA) { const int kb = r / 32, nb = r % 32; n0 = 64 * nb; k0 = 64 * kb; ldw = D; K = 512; scol = n0 + 4 * q4; W = a.w_out_a + (size_t)l * 512 * D; WT = ws + WS_WOA + (size_t)l * D * 512 * (MIX_F8 ? 1 : 2); if (MIX_F8) { d.f8 = 1; esz = 1; }
;                 if (BR_FUSE) { K = 1536; WT = ws + WS_WOA + (size_t)l * D * 1536 + 1024; }
;             } else if ((r -= C_OA) < C_OB) { const int kb = r / 32, nb = r % 32; n0 = 64 * nb; k0 = 64 * kb; ldw = D; K = 1024; scol = n0 + 4 * q4; W = a.w_out_b + (size_t)l * 1024 * D; WT = ws + WS_WOB + (size_t)l * D * 1024 * (MIX_F8 ? 1 : 2); if (MIX_F8) { d.f8 = 1; esz = 1; }
;                 if (BR_FUSE) { K = 1536; WT = ws + WS_WOA + (size_t)l * D * 1536; }
; template <unsigned MASK, bool ONE>
; __global__ void __launch_bounds__(NTHREADS, 2) fwd_kernel(Args a_unused) {
;     ...
;         if (IN(P + 1, 2)) { FRESH_TID();
;     ...
;             pg8::StaticOrderP S{T / 256, NP / 256, G, bx}; pg8::RowsContig AM; pg8::EpiProj E{proj, ropec, ropes, alow, pg8::W8_INV};
;             pg8::gemm_phase<pg8::EpiProj, pg8::StaticOrderP, pg8::RowsContig, true, true>(lds, tid, hbuf, (const bf16_t*)(ws + WS_WIN + (size_t)l * NP * D), 0, D / 2, S, AM, E);
.LBB0_265:
	s_or_b64 exec, exec, s[0:1]
	v_readlane_b32 s0, v253, 0
	v_readlane_b32 s1, v253, 1
	s_mov_b32 s2, s38
	s_waitcnt lgkmcnt(0)
	s_barrier
	s_nop 0
	v_mbcnt_lo_u32_b32 v0, s2, 0
	v_mbcnt_hi_u32_b32 v0, s2, v0
	v_readlane_b32 s2, v253, 7
	v_readlane_b32 s3, v253, 8
	v_add_u32_e32 v1, s78, v0
	s_andn2_b64 vcc, exec, s[2:3]
	v_readfirstlane_b32 s16, v1
	v_readlane_b32 s101, v255, 17
	s_movk_i32 s100, 0x100
	s_cmp_eq_u32 s101, 0
	s_cbranch_scc0 .Lpq_skip
	s_movk_i32 s100, 0xd8
	v_readlane_b32 s101, v253, 4
	s_nop 1
	s_cmp_lt_i32 s101, s100
	s_cbranch_scc1 .Lpq_skip
	s_mov_b32 s100, 0x7e80
	s_mov_b32 s101, 0xd680
	v_writelane_b32 v251, s16, 0
	v_writelane_b32 v251, s17, 1
	v_writelane_b32 v251, s18, 2
	v_writelane_b32 v251, s19, 3
	v_writelane_b32 v251, s20, 4
	v_writelane_b32 v251, s21, 5
	v_writelane_b32 v251, s23, 6
	v_writelane_b32 v251, s25, 7
	v_writelane_b32 v251, s26, 8
	v_writelane_b32 v251, s33, 9
	v_writelane_b32 v251, s38, 10
	v_writelane_b32 v251, s39, 11
	v_writelane_b32 v251, s41, 12
	v_writelane_b32 v251, s42, 13
	v_writelane_b32 v251, s45, 14
	v_writelane_b32 v251, s48, 15
	v_writelane_b32 v251, s49, 16
	v_writelane_b32 v251, s50, 17
	v_writelane_b32 v251, s51, 18
	v_writelane_b32 v251, s74, 19
	v_writelane_b32 v251, s76, 20
	v_mov_b32_e32 v193, v3
	v_mov_b32_e32 v194, v33
	v_mov_b32_e32 v195, v59
	v_mov_b32_e32 v196, v63
	v_mov_b32_e32 v197, v110
	v_mov_b32_e32 v198, v111
	v_mov_b32_e32 v199, v114
	v_mov_b32_e32 v200, v115
	v_mov_b32_e32 v201, v149
	v_mov_b32_e32 v202, v153
	v_mov_b32_e32 v203, v157
	v_mov_b32_e32 v204, v161
	v_mov_b32_e32 v205, v165
	v_mov_b32_e32 v206, v169
	v_mov_b32_e32 v207, v173
	v_mov_b32_e32 v208, v177
	v_mov_b32_e32 v209, v178
	v_mov_b32_e32 v210, v179
	v_mov_b32_e32 v211, v180
	v_mov_b32_e32 v212, v181
	v_mov_b32_e32 v214, v182
	v_mov_b32_e32 v215, v183
	v_mov_b32_e32 v216, v184
	v_mov_b32_e32 v218, v185
	v_readlane_b32 s76, v253, 4
	v_readlane_b32 s8, v253, 0
	v_readlane_b32 s9, v253, 1
	s_nop 1
	s_sub_i32 s0, s76, 216
	s_lshr_b32 s1, s100, 3
	s_add_i32 s0, s0, s1
	s_lshr_b32 s33, s78, 6
	s_lshr_b32 s1, s0, 3
	s_lshl_b32 s1, s1, 6
	s_and_b32 s0, s0, 7
	s_lshl_b32 s0, s0, 2
	s_or_b32 s1, s1, s0
	s_and_b32 s0, s33, 3
	s_or_b32 s1, s1, s0
	s_lshr_b32 s0, s33, 2
	s_lshl_b32 s0, s0, 5
	s_or_b32 s1, s1, s0
	s_sub_i32 s100, s1, s33
	s_mov_b32 s76, 0
	s_movk_i32 s74, 40
	s_load_dwordx2 s[10:11], s[8:9], 0xa0
	v_mbcnt_lo_u32_b32 v69, -1, 0
	v_mbcnt_hi_u32_b32 v69, -1, v69
	s_mov_b64 exec, -1
	v_lshlrev_b32_e32 v76, 3, v69
	s_waitcnt lgkmcnt(0)
	s_lshl_b32 s47, s76, 3
	s_add_i32 s47, s47, s33
	s_add_i32 s47, s47, s100
	v_and_b32_e32 v2, 15, v69
	s_cmp_ge_i32 s47, s101
	v_ashrrev_i32_e32 v133, 4, v69
	s_cbranch_scc1 .LBB0_36_hq
	s_sub_i32 s1, 0xfcff, s47
	s_mul_hi_u32 s0, s1, 0x81848da9
	s_lshr_b32 s0, s0, 14
	s_mul_i32 s2, s0, 0x7e80
	s_sub_i32 s17, s1, s2
	s_cmpk_gt_u32 s17, 0x177f
	s_cbranch_scc0 .LBB0_37_hq
	s_cmpk_gt_u32 s17, 0x187f
	s_cbranch_scc0 .LBB0_39_hq
	s_cmpk_gt_u32 s17, 0x1a7f
	s_cbranch_scc0 .LBB0_40_hq
	s_cmpk_gt_u32 s17, 0x1e7f
	s_cbranch_scc0 .LBB0_41_hq
	s_lshl_b32 s1, s17, 6
	s_cmpk_gt_u32 s17, 0x5e7f
	s_cbranch_scc0 .LBB0_42_hq
	s_add_i32 s2, s17, 0xffffa180
	s_lshr_b32 s4, s2, 9
	s_lshl_b32 s2, s2, 1
	s_and_b32 s18, s2, 0x3c0
	s_load_dwordx2 s[2:3], s[8:9], 0x88
	s_lshl_b32 s5, s0, 4
	s_add_i32 s6, s4, s5
	s_mov_b32 s7, 0
	s_and_b32 s16, s1, 0x7c0
	s_lshl_b64 s[4:5], s[6:7], 23
	s_waitcnt lgkmcnt(0)
	s_add_u32 s4, s2, s4
	s_addc_u32 s5, s3, s5
	s_lshl_b64 s[2:3], s[6:7], 21
	s_add_u32 s2, s10, s2
	s_addc_u32 s3, s11, s3
	s_add_u32 s6, s2, 0x18600000
	v_lshl_or_b32 v0, v2, 2, s16
	s_addc_u32 s7, s3, 0
	s_mov_b64 s[2:3], 0
	s_branch .LBB0_43_hq

;     ...
;         auto decode = [&](int it) -> TrDesc {
;             TrDesc d; d.zero = 0; d.rope = 0; d.f8 = 0;
;             const int l = it / C_L; int r = it % C_L;
;             const float* W; unsigned char* WT; int ldw, K, k0, n0, scol, esz = 2;
;             if (r < C_IN) { const int kb = r / 188, nb = r % 188; n0 = 64 * nb; k0 = 64 * kb; ldw = NIN; K = D; W = a.w_in + (size_t)l * D * NIN;
;                 if (n0 < 3072) { d.rope = 1; scol = (n0 >> 7) * 128 + 32 * ((n0 >> 6) & 1) + 64 * (q4 >> 3) + 4 * (q4 & 7); }
;                 else if (n0 < 7680) scol = n0 + 4 * q4;
;                 else if (n0 < 11776) scol = n0 + 16 + 4 * q4;
;                 else if (n0 == 11776) { scol = (q4 < 4) ? 7680 + 4 * q4 : 0; d.zero = (q4 < 4) ? 0 : 1; }
;                 else { scol = 0; d.zero = 1; }
;     ...
;                 d.f8 = 1; esz = 1; WT = ws + WS_WIN + (size_t)l * NP * D;
;     ...
;                 WT = ws + WS_WIN + (size_t)l * NP * D * 2;
;     ...
;             } else if ((r -= C_IN) < C_OA) { const int kb = r / 32, nb = r % 32; n0 = 64 * nb; k0 = 64 * kb; ldw = D; K = 512; scol = n0 + 4 * q4; W = a.w_out_a + (size_t)l * 512 * D; WT = ws + WS_WOA + (size_t)l * D * 512 * (MIX_F8 ? 1 : 2); if (MIX_F8) { d.f8 = 1; esz = 1; }
;                 if (BR_FUSE) { K = 1536; WT = ws + WS_WOA + (size_t)l * D * 1536 + 1024; }
;             } else if ((r -= C_OA) < C_OB) { const int kb = r / 32, nb = r % 32; n0 = 64 * nb; k0 = 64 * kb; ldw = D; K = 1024; scol = n0 + 4 * q4; W = a.w_out_b + (size_t)l * 1024 * D; WT = ws + WS_WOB + (size_t)l * D * 1024 * (MIX_F8 ? 1 : 2); if (MIX_F8) { d.f8 = 1; esz = 1; }
;                 if (BR_FUSE) { K = 1536; WT = ws + WS_WOA + (size_t)l * D * 1536; }
;             } else if ((r -= C_OB) < C_O) { const int kb = r / 32, nb = r % 32; n0 = 64 * nb; k0 = 64 * kb; ldw = D; K = D; scol = n0 + 4 * q4; W = a.w_out + (size_t)l * D * D; WT = ws + WS_WO + (size_t)l * D * D * (MIX_F8 ? 1 : 2); if (MIX_F8) { d.f8 = 1; esz = 1; }
;             } else if ((r -= C_O) < C_GU) { const int e = r / 1024, r2 = r % 1024, kb = r2 / 32, nb = r2 % 32, pn = nb >> 2, sgu = (nb >> 1) & 1, c0 = 64 * (nb & 1);
;                 n0 = 64 * nb; k0 = 64 * kb; ldw = FF; K = D; scol = 128 * pn + c0 + 4 * q4; W = (sgu ? a.w_up_e : a.w_gate_e) + (size_t)(l * NE + e) * D * FF; WT = ws + WS_WGU + (size_t)(l * NE + e) * 2048 * D; d.f8 = 1; esz = 1;
.LBB0_72_hq:
	s_cmp_ge_i32 s42, s101
	s_cbranch_scc1 .LBB0_70_hq
	s_lshr_b32 s44, s42, 6
	s_lshl_b32 s44, s44, 3
	s_bfe_u32 s100, s42, 0x30002
	s_or_b32 s44, s44, s100
	s_add_i32 s44, s44, 40
	s_and_b32 s100, s44, 7
	s_lshr_b32 s44, s44, 3
	s_lshl_b32 s44, s44, 6
	s_lshl_b32 s100, s100, 2
	s_or_b32 s44, s44, s100
	s_and_b32 s100, s42, 0x23
	s_or_b32 s44, s44, s100
	s_cmp_lt_i32 s44, s101
	s_cselect_b64 s[20:21], -1, 0
	s_cmp_ge_i32 s44, s101
	s_cselect_b64 s[12:13], -1, 0
	s_and_b64 vcc, exec, s[12:13]
	s_cbranch_vccnz .LBB0_106_hq
	s_sub_i32 s3, 0xfcff, s44
	s_mul_hi_u32 s0, s3, 0x81848da9
	s_lshr_b32 s0, s0, 14
	s_mul_i32 s14, s0, 0x7e80
	s_sub_i32 s45, s3, s14
	s_cmpk_gt_u32 s45, 0x177f
	s_cbranch_scc0 .LBB0_81_hq
	s_cmpk_gt_u32 s45, 0x187f
	s_cbranch_scc0 .LBB0_83_hq
	s_cmpk_gt_u32 s45, 0x1a7f
	s_cbranch_scc0 .LBB0_84_hq
	s_cmpk_gt_u32 s45, 0x1e7f
	s_cbranch_scc0 .LBB0_85_hq
	s_lshl_b32 s24, s45, 6
	s_cmpk_gt_u32 s45, 0x5e7f
	s_cbranch_scc0 .LBB0_121_hq
	s_add_i32 s14, s45, 0xffffa180
	s_lshr_b32 s18, s14, 9
	s_lshl_b32 s14, s14, 1
	s_and_b32 s49, s14, 0x3c0
	s_load_dwordx2 s[14:15], s[8:9], 0x88
	s_lshl_b32 s19, s0, 4
	s_add_i32 s22, s18, s19
	s_mov_b32 s23, s1
	s_and_b32 s3, s24, 0x7c0
	s_lshl_b64 s[18:19], s[22:23], 23
	s_waitcnt lgkmcnt(0)
	s_add_u32 s18, s14, s18
	s_addc_u32 s19, s15, s19
	s_lshl_b64 s[14:15], s[22:23], 21
	s_add_u32 s22, s28, s14
	v_or_b32_e32 v0, s3, v136
	s_addc_u32 s23, s29, s15
	s_cbranch_execz .LBB0_122_hq
	s_movk_i32 s14, 0x400
	s_mov_b64 s[24:25], 0x800
	s_cbranch_execz .LBB0_86_hq
	s_branch .LBB0_87_hq

; #define LAS __attribute__((address_space(3)))
; #define GAS __attribute__((address_space(1)))
; #define LDS_WAIT() asm volatile("s_waitcnt lgkmcnt(0)" ::: "memory")
; __device__ __forceinline__ unsigned pk_fp8x4(float a, float b, float c, float d) { int p = __builtin_amdgcn_cvt_pk_fp8_f32(sat8(a), sat8(b), 0, false); p = __builtin_amdgcn_cvt_pk_fp8_f32(sat8(c), sat8(d), p, true); return (unsigned)p; }
; __device__ __forceinline__ void tr_finish(const TrDesc& d, f32x4 (&v)[16], LAS float* scr, int lane) {
;     const int kk = lane >> 4, q4 = lane & 15;
;     if (d.zero) {
; #pragma unroll
;         for (int i = 0; i < 16; ++i) v[i] = (f32x4){0.f, 0.f, 0.f, 0.f}; }
;     const int d0 = d.rope ? 8 * (q4 & 7) + (q4 >> 3) : 4 * q4, ds = d.rope ? 2 : 1;
;     { LAS float* rp = scr + kk * 65 + d0;
; #pragma unroll
;         for (int i = 0; i < 16; ++i) { rp[4 * i * 65] = v[i][0]; rp[4 * i * 65 + ds] = v[i][1]; rp[4 * i * 65 + 2 * ds] = v[i][2]; rp[4 * i * 65 + 3 * ds] = v[i][3]; } }
;     LDS_WAIT(); asm volatile("" ::: "memory");
;     if (d.f8) {
;         const int c = lane & 3, nl = lane >> 2; const LAS float* sp = scr + (16 * c) * 65 + nl; unsigned char* dp = d.dst + (size_t)nl * d.K + 16 * c;
; #pragma unroll
;         for (int j = 0; j < 4; ++j) { u32x4 o;
;             o.x = pk_fp8x4(sp[0 * 65 + 16 * j] * 32.0f, sp[1 * 65 + 16 * j] * 32.0f, sp[2 * 65 + 16 * j] * 32.0f, sp[3 * 65 + 16 * j] * 32.0f);
;             o.y = pk_fp8x4(sp[4 * 65 + 16 * j] * 32.0f, sp[5 * 65 + 16 * j] * 32.0f, sp[6 * 65 + 16 * j] * 32.0f, sp[7 * 65 + 16 * j] * 32.0f);
;             o.z = pk_fp8x4(sp[8 * 65 + 16 * j] * 32.0f, sp[9 * 65 + 16 * j] * 32.0f, sp[10 * 65 + 16 * j] * 32.0f, sp[11 * 65 + 16 * j] * 32.0f);
;             o.w = pk_fp8x4(sp[12 * 65 + 16 * j] * 32.0f, sp[13 * 65 + 16 * j] * 32.0f, sp[14 * 65 + 16 * j] * 32.0f, sp[15 * 65 + 16 * j] * 32.0f);
;             *(GAS u32x4*)(dp + (size_t)(16 * j) * d.K) = o; }
.LBB0_108_hq:
	s_or_b64 exec, exec, s[22:23]
	s_cmp_eq_u32 s43, 0
	s_cselect_b64 vcc, -1, 0
	s_cmp_lg_u32 s43, 0
	s_cselect_b64 s[22:23], -1, 0
	v_cndmask_b32_e64 v2, 0, 1, s[22:23]
	s_and_b64 s[22:23], s[22:23], exec
	v_cndmask_b32_e32 v0, v140, v136, vcc
	s_cselect_b32 s0, 2, 1
	v_lshl_add_u32 v0, v0, 2, v141
	s_lshl_b32 s3, s0, 2
	v_add_u32_e32 v3, s3, v0
	v_lshlrev_b32_e64 v2, v2, 3
	s_waitcnt vmcnt(15)
	ds_write_b32 v3, v5
	v_lshl_add_u32 v3, s0, 3, v0
	v_lshl_add_u32 v2, v2, 2, v0
	v_subrev_u32_e32 v146, s3, v3
	ds_write_b32 v0, v4
	ds_write_b32 v3, v6
	ds_write_b32 v2, v7
	s_waitcnt vmcnt(14)
	ds_write_b32 v0, v8 offset:1040
	ds_write_b32 v146, v9 offset:1040
	ds_write_b32 v3, v10 offset:1040
	ds_write_b32 v2, v11 offset:1040
	s_waitcnt vmcnt(13)
	ds_write_b32 v0, v12 offset:2080
	ds_write_b32 v146, v13 offset:2080
	ds_write_b32 v3, v14 offset:2080
	ds_write_b32 v2, v15 offset:2080
	s_waitcnt vmcnt(12)
	ds_write_b32 v0, v16 offset:3120
	ds_write_b32 v146, v17 offset:3120
	ds_write_b32 v3, v18 offset:3120
	ds_write_b32 v2, v19 offset:3120
	s_waitcnt vmcnt(11)
	ds_write_b32 v0, v20 offset:4160
	ds_write_b32 v146, v21 offset:4160
	ds_write_b32 v3, v22 offset:4160
	ds_write_b32 v2, v23 offset:4160
	s_waitcnt vmcnt(10)
	ds_write_b32 v0, v24 offset:5200
	ds_write_b32 v146, v25 offset:5200
	ds_write_b32 v3, v26 offset:5200
	ds_write_b32 v2, v27 offset:5200
	s_waitcnt vmcnt(9)
	ds_write_b32 v0, v28 offset:6240
	ds_write_b32 v146, v29 offset:6240
	ds_write_b32 v3, v30 offset:6240
	ds_write_b32 v2, v31 offset:6240
	s_waitcnt vmcnt(8)
	ds_write_b32 v0, v32 offset:7280
	ds_write_b32 v146, v33 offset:7280
	ds_write_b32 v3, v34 offset:7280
	ds_write_b32 v2, v35 offset:7280
	s_waitcnt vmcnt(7)
	ds_write_b32 v0, v36 offset:8320
	ds_write_b32 v146, v37 offset:8320
	ds_write_b32 v3, v38 offset:8320
	ds_write_b32 v2, v39 offset:8320
	s_waitcnt vmcnt(6)
	ds_write_b32 v0, v40 offset:9360
	ds_write_b32 v146, v41 offset:9360
	ds_write_b32 v3, v42 offset:9360
	ds_write_b32 v2, v43 offset:9360
	s_waitcnt vmcnt(5)
	ds_write_b32 v0, v44 offset:10400
	ds_write_b32 v146, v45 offset:10400
	ds_write_b32 v3, v46 offset:10400
	ds_write_b32 v2, v47 offset:10400
	s_waitcnt vmcnt(4)
	ds_write_b32 v0, v48 offset:11440
	ds_write_b32 v146, v49 offset:11440
	ds_write_b32 v3, v50 offset:11440
	ds_write_b32 v2, v51 offset:11440
	s_waitcnt vmcnt(3)
	ds_write_b32 v0, v52 offset:12480
	ds_write_b32 v146, v53 offset:12480
	ds_write_b32 v3, v54 offset:12480
	ds_write_b32 v2, v55 offset:12480
	s_waitcnt vmcnt(2)
	ds_write_b32 v0, v56 offset:13520
	ds_write_b32 v146, v57 offset:13520
	ds_write_b32 v3, v58 offset:13520
	ds_write_b32 v2, v59 offset:13520
	s_waitcnt vmcnt(1)
	ds_write_b32 v0, v60 offset:14560
	ds_write_b32 v146, v61 offset:14560
	ds_write_b32 v3, v62 offset:14560
	ds_write_b32 v2, v63 offset:14560
	s_waitcnt vmcnt(0)
	ds_write_b32 v0, v64 offset:15600
	ds_write_b32 v146, v65 offset:15600
	ds_write_b32 v3, v66 offset:15600
	ds_write_b32 v2, v67 offset:15600
	s_waitcnt lgkmcnt(0)
	ds_read2_b32 v[2:3], v142 offset1:16
	ds_read2_b32 v[148:149], v142 offset0:65 offset1:81
	ds_read2_b32 v[154:155], v142 offset0:130 offset1:146
	ds_read2_b32 v[156:157], v142 offset0:195 offset1:211
	v_mov_b32_e32 v150, 0
	s_waitcnt lgkmcnt(3)
	v_mul_f32_e32 v0, 0x42000000, v2
	s_waitcnt lgkmcnt(2)
	v_mul_f32_e32 v2, 0x42000000, v148
	v_med3_f32 v0, v0, s41, v143
	s_waitcnt lgkmcnt(0)
	v_mul_f32_e32 v147, 0x42000000, v156
	v_med3_f32 v2, v2, s41, v143
	v_cvt_pk_fp8_f32 v150, v0, v2
	v_med3_f32 v2, v147, s41, v143
	v_add_u32_e32 v147, 0x400, v142
	ds_read2_b32 v[160:161], v147 offset0:4 offset1:20
	ds_read2_b32 v[162:163], v147 offset0:69 offset1:85
	ds_read2_b32 v[164:165], v147 offset0:134 offset1:150
	ds_read2_b32 v[166:167], v147 offset0:199 offset1:215
	v_mul_f32_e32 v146, 0x42000000, v154
	v_med3_f32 v0, v146, s41, v143
	v_cvt_pk_fp8_f32 v150, v0, v2 op_sel:[0,0,1]
	s_waitcnt lgkmcnt(3)
	v_mul_f32_e32 v0, 0x42000000, v160
	s_waitcnt lgkmcnt(2)
	v_mul_f32_e32 v2, 0x42000000, v162
	s_waitcnt lgkmcnt(0)
	v_mul_f32_e32 v148, 0x42000000, v166
	v_med3_f32 v0, v0, s41, v143
	v_med3_f32 v2, v2, s41, v143
	v_mov_b32_e32 v151, 0
	v_cvt_pk_fp8_f32 v151, v0, v2
	v_med3_f32 v2, v148, s41, v143
	v_add_u32_e32 v148, 0x800, v142
	ds_read2_b32 v[168:169], v148 offset0:8 offset1:24
	ds_read2_b32 v[170:171], v148 offset0:73 offset1:89
	ds_read2_b32 v[172:173], v148 offset0:138 offset1:154
	ds_read2_b32 v[174:175], v148 offset0:203 offset1:219
	v_mul_f32_e32 v146, 0x42000000, v164
	v_med3_f32 v0, v146, s41, v143
	v_cvt_pk_fp8_f32 v151, v0, v2 op_sel:[0,0,1]
	s_waitcnt lgkmcnt(3)
	v_mul_f32_e32 v0, 0x42000000, v168
	s_waitcnt lgkmcnt(2)
	v_mul_f32_e32 v2, 0x42000000, v170
	s_waitcnt lgkmcnt(1)
	v_mul_f32_e32 v146, 0x42000000, v172
	v_med3_f32 v0, v0, s41, v143
	v_med3_f32 v2, v2, s41, v143
	v_mov_b32_e32 v152, 0
	v_cvt_pk_fp8_f32 v152, v0, v2
	v_med3_f32 v0, v146, s41, v143
	v_add_u32_e32 v146, 0xc00, v142
	ds_read2_b32 v[176:177], v146 offset0:12 offset1:28
	ds_read2_b32 v[178:179], v146 offset0:77 offset1:93
	ds_read2_b32 v[180:181], v146 offset0:142 offset1:158
	s_waitcnt lgkmcnt(3)
	v_mul_f32_e32 v153, 0x42000000, v174
	v_med3_f32 v2, v153, s41, v143
	ds_read2_b32 v[182:183], v146 offset0:207 offset1:223
	v_cvt_pk_fp8_f32 v152, v0, v2 op_sel:[0,0,1]
	s_waitcnt lgkmcnt(3)
	v_mul_f32_e32 v0, 0x42000000, v176
	s_waitcnt lgkmcnt(2)
	v_mul_f32_e32 v2, 0x42000000, v178
	v_med3_f32 v0, v0, s41, v143
	v_med3_f32 v2, v2, s41, v143
	v_mov_b32_e32 v153, 0
	v_cvt_pk_fp8_f32 v153, v0, v2
	s_waitcnt lgkmcnt(1)
	v_mul_f32_e32 v154, 0x42000000, v180
	s_waitcnt lgkmcnt(0)
; #define GAS __attribute__((address_space(1)))
; __device__ __forceinline__ unsigned pk_fp8x4(float a, float b, float c, float d) { int p = __builtin_amdgcn_cvt_pk_fp8_f32(sat8(a), sat8(b), 0, false); p = __builtin_amdgcn_cvt_pk_fp8_f32(sat8(c), sat8(d), p, true); return (unsigned)p; }
; __device__ __forceinline__ void tr_finish(const TrDesc& d, f32x4 (&v)[16], LAS float* scr, int lane) {
;     ...
;         for (int j = 0; j < 4; ++j) { u32x4 o;
;             o.x = pk_fp8x4(sp[0 * 65 + 16 * j] * 32.0f, sp[1 * 65 + 16 * j] * 32.0f, sp[2 * 65 + 16 * j] * 32.0f, sp[3 * 65 + 16 * j] * 32.0f);
;             o.y = pk_fp8x4(sp[4 * 65 + 16 * j] * 32.0f, sp[5 * 65 + 16 * j] * 32.0f, sp[6 * 65 + 16 * j] * 32.0f, sp[7 * 65 + 16 * j] * 32.0f);
;             o.z = pk_fp8x4(sp[8 * 65 + 16 * j] * 32.0f, sp[9 * 65 + 16 * j] * 32.0f, sp[10 * 65 + 16 * j] * 32.0f, sp[11 * 65 + 16 * j] * 32.0f);
;             o.w = pk_fp8x4(sp[12 * 65 + 16 * j] * 32.0f, sp[13 * 65 + 16 * j] * 32.0f, sp[14 * 65 + 16 * j] * 32.0f, sp[15 * 65 + 16 * j] * 32.0f);
;             *(GAS u32x4*)(dp + (size_t)(16 * j) * d.K) = o; }
;     ...
;             if (itB >= NIT) break;
	v_mul_f32_e32 v0, 0x42000000, v182
	v_med3_f32 v2, v154, s41, v143
	v_med3_f32 v0, v0, s41, v143
	v_cvt_pk_fp8_f32 v153, v2, v0 op_sel:[0,0,1]
	v_mov_b64_e32 v[158:159], s[16:17]
	v_mad_i64_i32 v[158:159], s[22:23], s2, v132, v[158:159]
	v_lshl_add_u64 v[158:159], v[158:159], 0, v[134:135]
	v_mul_f32_e32 v0, 0x42000000, v3
	v_mul_f32_e32 v2, 0x42000000, v149
	global_store_dwordx4 v[158:159], v[150:153], off
	v_med3_f32 v0, v0, s41, v143
	v_med3_f32 v2, v2, s41, v143
	v_mov_b32_e32 v150, 0
	v_cvt_pk_fp8_f32 v150, v0, v2
	v_mul_f32_e32 v3, 0x42000000, v155
	v_mul_f32_e32 v0, 0x42000000, v157
	v_med3_f32 v2, v3, s41, v143
	v_med3_f32 v0, v0, s41, v143
	v_cvt_pk_fp8_f32 v150, v2, v0 op_sel:[0,0,1]
	v_mul_f32_e32 v0, 0x42000000, v161
	v_mul_f32_e32 v2, 0x42000000, v163
	v_med3_f32 v0, v0, s41, v143
	v_med3_f32 v2, v2, s41, v143
	v_mov_b32_e32 v151, 0
	v_cvt_pk_fp8_f32 v151, v0, v2
	v_mul_f32_e32 v3, 0x42000000, v165
	v_mul_f32_e32 v0, 0x42000000, v167
	v_med3_f32 v2, v3, s41, v143
	v_med3_f32 v0, v0, s41, v143
	v_cvt_pk_fp8_f32 v151, v2, v0 op_sel:[0,0,1]
	v_mul_f32_e32 v0, 0x42000000, v169
	v_mul_f32_e32 v2, 0x42000000, v171
	v_med3_f32 v0, v0, s41, v143
	v_med3_f32 v2, v2, s41, v143
	v_mov_b32_e32 v152, 0
	v_cvt_pk_fp8_f32 v152, v0, v2
	v_mul_f32_e32 v3, 0x42000000, v173
	v_mul_f32_e32 v0, 0x42000000, v175
	v_med3_f32 v2, v3, s41, v143
	v_med3_f32 v0, v0, s41, v143
	v_cvt_pk_fp8_f32 v152, v2, v0 op_sel:[0,0,1]
	v_mul_f32_e32 v0, 0x42000000, v177
	v_mul_f32_e32 v2, 0x42000000, v179
	v_med3_f32 v0, v0, s41, v143
	v_med3_f32 v2, v2, s41, v143
	v_mov_b32_e32 v153, 0
	v_cvt_pk_fp8_f32 v153, v0, v2
	s_ashr_i32 s3, s2, 31
	v_mul_f32_e32 v3, 0x42000000, v181
	v_mul_f32_e32 v0, 0x42000000, v183
	v_med3_f32 v2, v3, s41, v143
	v_med3_f32 v0, v0, s41, v143
	s_lshl_b64 s[22:23], s[2:3], 4
	v_cvt_pk_fp8_f32 v153, v2, v0 op_sel:[0,0,1]
	v_lshl_add_u64 v[2:3], v[158:159], 0, s[22:23]
	ds_read2_b32 v[154:155], v142 offset0:32 offset1:48
	ds_read2_b32 v[156:157], v142 offset0:97 offset1:113
	ds_read2_b32 v[158:159], v142 offset0:162 offset1:178
	ds_read2_b32 v[160:161], v142 offset0:227 offset1:243
	s_andn2_b64 vcc, exec, s[20:21]
	s_waitcnt lgkmcnt(3)
	v_mul_f32_e32 v0, 0x42000000, v154
	s_waitcnt lgkmcnt(2)
	v_mul_f32_e32 v149, 0x42000000, v156
	global_store_dwordx4 v[2:3], v[150:153], off
	v_med3_f32 v0, v0, s41, v143
	v_med3_f32 v149, v149, s41, v143
	v_mov_b32_e32 v150, 0
	v_cvt_pk_fp8_f32 v150, v0, v149
	ds_read2_b32 v[162:163], v147 offset0:36 offset1:52
	ds_read2_b32 v[164:165], v147 offset0:101 offset1:117
	ds_read2_b32 v[166:167], v147 offset0:166 offset1:182
	ds_read2_b32 v[168:169], v147 offset0:231 offset1:247
	s_waitcnt lgkmcnt(5)
	v_mul_f32_e32 v151, 0x42000000, v158
	s_waitcnt lgkmcnt(4)
	v_mul_f32_e32 v152, 0x42000000, v160
	v_med3_f32 v0, v151, s41, v143
	v_med3_f32 v149, v152, s41, v143
	v_cvt_pk_fp8_f32 v150, v0, v149 op_sel:[0,0,1]
	s_waitcnt lgkmcnt(3)
	v_mul_f32_e32 v0, 0x42000000, v162
	s_waitcnt lgkmcnt(2)
	v_mul_f32_e32 v149, 0x42000000, v164
	v_med3_f32 v0, v0, s41, v143
	v_med3_f32 v149, v149, s41, v143
	v_mov_b32_e32 v151, 0
	v_cvt_pk_fp8_f32 v151, v0, v149
	ds_read2_b32 v[170:171], v148 offset0:40 offset1:56
	ds_read2_b32 v[172:173], v148 offset0:105 offset1:121
	ds_read2_b32 v[174:175], v148 offset0:170 offset1:186
	ds_read2_b32 v[176:177], v148 offset0:235 offset1:251
	s_waitcnt lgkmcnt(5)
	v_mul_f32_e32 v152, 0x42000000, v166
	s_waitcnt lgkmcnt(4)
	v_mul_f32_e32 v153, 0x42000000, v168
	v_med3_f32 v0, v152, s41, v143
	v_med3_f32 v149, v153, s41, v143
	v_cvt_pk_fp8_f32 v151, v0, v149 op_sel:[0,0,1]
	s_waitcnt lgkmcnt(3)
	v_mul_f32_e32 v0, 0x42000000, v170
	s_waitcnt lgkmcnt(2)
	v_mul_f32_e32 v149, 0x42000000, v172
	v_med3_f32 v0, v0, s41, v143
	v_med3_f32 v149, v149, s41, v143
	v_mov_b32_e32 v152, 0
	v_cvt_pk_fp8_f32 v152, v0, v149
	ds_read2_b32 v[178:179], v146 offset0:44 offset1:60
	ds_read2_b32 v[180:181], v146 offset0:109 offset1:125
	ds_read2_b32 v[182:183], v146 offset0:174 offset1:190
	s_waitcnt lgkmcnt(4)
	v_mul_f32_e32 v153, 0x42000000, v174
	s_waitcnt lgkmcnt(3)
	v_mul_f32_e32 v154, 0x42000000, v176
	v_med3_f32 v0, v153, s41, v143
	v_med3_f32 v149, v154, s41, v143
	ds_read2_b32 v[184:185], v146 offset0:239 offset1:255
	v_cvt_pk_fp8_f32 v152, v0, v149 op_sel:[0,0,1]
	s_waitcnt lgkmcnt(3)
	v_mul_f32_e32 v0, 0x42000000, v178
	s_waitcnt lgkmcnt(2)
	v_mul_f32_e32 v149, 0x42000000, v180
	v_med3_f32 v0, v0, s41, v143
	v_med3_f32 v149, v149, s41, v143
	v_mov_b32_e32 v153, 0
	v_cvt_pk_fp8_f32 v153, v0, v149
	s_waitcnt lgkmcnt(1)
	v_mul_f32_e32 v154, 0x42000000, v182
	s_waitcnt lgkmcnt(0)
	v_mul_f32_e32 v0, 0x42000000, v184
	v_med3_f32 v149, v154, s41, v143
	v_med3_f32 v0, v0, s41, v143
	v_cvt_pk_fp8_f32 v153, v149, v0 op_sel:[0,0,1]
	v_mul_f32_e32 v0, 0x42000000, v155
	v_mul_f32_e32 v149, 0x42000000, v157
	v_med3_f32 v0, v0, s41, v143
	v_med3_f32 v149, v149, s41, v143
	v_mov_b32_e32 v154, 0
	v_cvt_pk_fp8_f32 v154, v0, v149
	v_mul_f32_e32 v155, 0x42000000, v159
	v_mul_f32_e32 v0, 0x42000000, v161
	v_med3_f32 v149, v155, s41, v143
	v_med3_f32 v0, v0, s41, v143
	v_cvt_pk_fp8_f32 v154, v149, v0 op_sel:[0,0,1]
	v_mul_f32_e32 v0, 0x42000000, v163
	v_mul_f32_e32 v149, 0x42000000, v165
	v_med3_f32 v0, v0, s41, v143
	v_med3_f32 v149, v149, s41, v143
	v_mov_b32_e32 v155, 0
	v_cvt_pk_fp8_f32 v155, v0, v149
	v_mul_f32_e32 v156, 0x42000000, v167
	v_mul_f32_e32 v0, 0x42000000, v169
	v_med3_f32 v149, v156, s41, v143
	v_med3_f32 v0, v0, s41, v143
	v_cvt_pk_fp8_f32 v155, v149, v0 op_sel:[0,0,1]
	v_mul_f32_e32 v0, 0x42000000, v171
	v_mul_f32_e32 v149, 0x42000000, v173
	v_med3_f32 v0, v0, s41, v143
	v_med3_f32 v149, v149, s41, v143
	v_mov_b32_e32 v156, 0
	v_cvt_pk_fp8_f32 v156, v0, v149
	v_mul_f32_e32 v157, 0x42000000, v175
	v_mul_f32_e32 v0, 0x42000000, v177
	v_med3_f32 v149, v157, s41, v143
	v_med3_f32 v0, v0, s41, v143
	v_cvt_pk_fp8_f32 v156, v149, v0 op_sel:[0,0,1]
	v_mul_f32_e32 v0, 0x42000000, v179
	v_mul_f32_e32 v149, 0x42000000, v181
	v_med3_f32 v0, v0, s41, v143
	v_med3_f32 v149, v149, s41, v143
	v_mov_b32_e32 v157, 0
	v_cvt_pk_fp8_f32 v157, v0, v149
	v_mul_f32_e32 v158, 0x42000000, v183
	v_mul_f32_e32 v0, 0x42000000, v185
	v_med3_f32 v149, v158, s41, v143
	v_med3_f32 v0, v0, s41, v143
	v_cvt_pk_fp8_f32 v157, v149, v0 op_sel:[0,0,1]
	v_lshl_add_u64 v[2:3], v[2:3], 0, s[22:23]
	global_store_dwordx4 v[2:3], v[150:153], off
	v_lshl_add_u64 v[2:3], v[2:3], 0, s[22:23]
	global_store_dwordx4 v[2:3], v[154:157], off
	s_waitcnt lgkmcnt(0)
	s_cbranch_vccnz .LBB0_71_hq
;     ...
;         auto decode = [&](int it) -> TrDesc {
;             TrDesc d; d.zero = 0; d.rope = 0; d.f8 = 0;
;             const int l = it / C_L; int r = it % C_L;
;             const float* W; unsigned char* WT; int ldw, K, k0, n0, scol, esz = 2;
;             if (r < C_IN) { const int kb = r / 188, nb = r % 188; n0 = 64 * nb; k0 = 64 * kb; ldw = NIN; K = D; W = a.w_in + (size_t)l * D * NIN;
;                 if (n0 < 3072) { d.rope = 1; scol = (n0 >> 7) * 128 + 32 * ((n0 >> 6) & 1) + 64 * (q4 >> 3) + 4 * (q4 & 7); }
;                 else if (n0 < 7680) scol = n0 + 4 * q4;
;                 else if (n0 < 11776) scol = n0 + 16 + 4 * q4;
;                 else if (n0 == 11776) { scol = (q4 < 4) ? 7680 + 4 * q4 : 0; d.zero = (q4 < 4) ? 0 : 1; }
;                 else { scol = 0; d.zero = 1; }
;     ...
;                 d.f8 = 1; esz = 1; WT = ws + WS_WIN + (size_t)l * NP * D;
;     ...
;                 WT = ws + WS_WIN + (size_t)l * NP * D * 2;
;     ...
;             } else if ((r -= C_IN) < C_OA) { const int kb = r / 32, nb = r % 32; n0 = 64 * nb; k0 = 64 * kb; ldw = D; K = 512; scol = n0 + 4 * q4; W = a.w_out_a + (size_t)l * 512 * D; WT = ws + WS_WOA + (size_t)l * D * 512 * (MIX_F8 ? 1 : 2); if (MIX_F8) { d.f8 = 1; esz = 1; }
;                 if (BR_FUSE) { K = 1536; WT = ws + WS_WOA + (size_t)l * D * 1536 + 1024; }
;             } else if ((r -= C_OA) < C_OB) { const int kb = r / 32, nb = r % 32; n0 = 64 * nb; k0 = 64 * kb; ldw = D; K = 1024; scol = n0 + 4 * q4; W = a.w_out_b + (size_t)l * 1024 * D; WT = ws + WS_WOB + (size_t)l * D * 1024 * (MIX_F8 ? 1 : 2); if (MIX_F8) { d.f8 = 1; esz = 1; }
;                 if (BR_FUSE) { K = 1536; WT = ws + WS_WOA + (size_t)l * D * 1536; }
;             } else if ((r -= C_OB) < C_O) { const int kb = r / 32, nb = r % 32; n0 = 64 * nb; k0 = 64 * kb; ldw = D; K = D; scol = n0 + 4 * q4; W = a.w_out + (size_t)l * D * D; WT = ws + WS_WO + (size_t)l * D * D * (MIX_F8 ? 1 : 2); if (MIX_F8) { d.f8 = 1; esz = 1; }
;             } else if ((r -= C_O) < C_GU) { const int e = r / 1024, r2 = r % 1024, kb = r2 / 32, nb = r2 % 32, pn = nb >> 2, sgu = (nb >> 1) & 1, c0 = 64 * (nb & 1);
;                 n0 = 64 * nb; k0 = 64 * kb; ldw = FF; K = D; scol = 128 * pn + c0 + 4 * q4; W = (sgu ? a.w_up_e : a.w_gate_e) + (size_t)(l * NE + e) * D * FF; WT = ws + WS_WGU + (size_t)(l * NE + e) * 2048 * D; d.f8 = 1; esz = 1;
	s_lshr_b32 s42, s44, 6
	s_lshl_b32 s42, s42, 3
	s_bfe_u32 s100, s44, 0x30002
	s_or_b32 s42, s42, s100
	s_add_i32 s42, s42, 40
	s_and_b32 s100, s42, 7
	s_lshr_b32 s42, s42, 3
	s_lshl_b32 s42, s42, 6
	s_lshl_b32 s100, s100, 2
	s_or_b32 s42, s42, s100
	s_and_b32 s100, s44, 0x23
	s_or_b32 s42, s42, s100
	s_cmp_ge_i32 s42, s101
	s_cbranch_scc1 .LBB0_144_hq
	s_sub_i32 s2, 0xfcff, s42
	s_mul_hi_u32 s0, s2, 0x81848da9
	s_lshr_b32 s0, s0, 14
	s_mul_i32 s3, s0, 0x7e80
	s_sub_i32 s27, s2, s3
	s_cmpk_gt_u32 s27, 0x177f
	s_cbranch_scc0 .LBB0_117_hq
	s_cmpk_gt_u32 s27, 0x187f
	s_cbranch_scc0 .LBB0_119_hq
	s_cmpk_gt_u32 s27, 0x1a7f
	s_cbranch_scc0 .LBB0_120_hq
	s_cmpk_gt_u32 s27, 0x1e7f
	s_cbranch_scc0 .LBB0_123_hq
	s_lshl_b32 s22, s27, 6
	s_cmpk_gt_u32 s27, 0x5e7f
	s_cbranch_scc0 .LBB0_147_hq
	s_add_i32 s2, s27, 0xffffa180
	s_lshr_b32 s16, s2, 9
	s_lshl_b32 s2, s2, 1
	s_and_b32 s44, s2, 0x3c0
	s_load_dwordx2 s[2:3], s[8:9], 0x88
	s_lshl_b32 s17, s0, 4
	s_add_i32 s20, s16, s17
	s_mov_b32 s21, s1
	s_and_b32 s15, s22, 0x7c0
	s_lshl_b64 s[16:17], s[20:21], 23
	s_waitcnt lgkmcnt(0)
	s_add_u32 s16, s2, s16
	s_addc_u32 s17, s3, s17
	s_lshl_b64 s[2:3], s[20:21], 21
	s_add_u32 s20, s28, s2
	v_or_b32_e32 v0, s15, v136
	s_addc_u32 s21, s29, s3
	s_cbranch_execz .LBB0_148_hq
	s_movk_i32 s2, 0x400
	s_mov_b64 s[22:23], 0x800
	s_cbranch_execz .LBB0_124_hq
	s_branch .LBB0_125_hq

; #define PG8_BAR __builtin_amdgcn_s_barrier()
; template <class Epi, class Sched, class AMap, bool ALIGN_EPI, bool F8 = false, bool SEG2 = false>
; __device__ __forceinline__ void gemm_phase(LAS unsigned char* lds, const int tid, const bf16_t* A, const bf16_t* Bt, size_t bstride, int K, const Sched& S, const AMap& AM, const Epi& E) {
;     ...
;     for (int i = 0; i < 2; ++i) { int R, C; stage_rc(tid * 16 + i * 8192, R, C); const int Rb = Epi::PERM ? ((R & ~31) + perm32(R & 31)) : R; voffA[i] = (unsigned)(R * K + C) * 2u; voffB[i] = (unsigned)(Rb * K + C) * 2u; }
;     const unsigned kstep = (unsigned)(BK * 2);
;     const unsigned hstep = (unsigned)HALF * (unsigned)K * 2u;
;     const unsigned tstep = 2u * hstep;
;     const __amdgpu_buffer_rsrc_t rsA = __builtin_amdgcn_make_buffer_rsrc((void*)A, 0, -1, 0x00020000), rsB = __builtin_amdgcn_make_buffer_rsrc((void*)Bt, 0, -1, 0x00020000);
;     const unsigned ldsw = (unsigned)wid * 1024u;
;     const int aoff = lds_byte(wr * 64 + fr, fq * 8), boff = lds_byte(wc * 32 + fr, fq * 8);
;     ...
;     Unit cur, nxt, nn; int ui = 0; bool has_next = false, has_nn = false;
;     if (!S.next(0, cur)) return;
;     f32x4 acc[2][2][4][2];
; #pragma unroll
;     for (int a = 0; a < 2; ++a)
; #pragma unroll
;         for (int b = 0; b < 2; ++b)
; #pragma unroll
;             for (int m = 0; m < 4; ++m)
; #pragma unroll
;                 for (int n = 0; n < 2; ++n) acc[a][b][m][n] = (f32x4){0.f, 0.f, 0.f, 0.f};
;     bf16x8 At[4][2], B0[2][2], B1[2][2]; i32x8 At8[4], B08[2], B18[2];
;     int sc8 = 0x7F7F7F7F; if constexpr (F8) asm volatile("" : "+v"(sc8));
;     ...
;     unsigned offC[2][2], offN[2][2], rawN[2][2];
;     if constexpr (AMap::GATHER) { PG8_OFFS(offC, cur); has_next = S.next(1, nxt);
;         if (has_next) { PG8_RAW(rawN, nxt); } else {
; #pragma unroll
;             for (int h = 0; h < 2; ++h)
; #pragma unroll
;                 for (int i = 0; i < 2; ++i) rawN[h][i] = 0u; } }
;     unsigned cA = AMap::GATHER ? 0u : (unsigned)cur.pm * tstep + (SEG2 ? (unsigned)cur.e * 1024u : 0u), nA = cA;
;     unsigned cB = (unsigned)cur.e * (SEG2 ? 1024u : (unsigned)(bstride * 2)) + (unsigned)cur.pn * tstep;
;     PG8_STAGE(PG8_SB(0, 0), cB, voffB); PG8_STAGE(PG8_SB(0, 1), cB + hstep, voffB); PG8_STAGE_A(PG8_SA(0, 0), 0, 0, false); PG8_STAGE_A(PG8_SA(0, 1), 1, 0, false);
;     if (wr == 1) PG8_BAR;
;     PG8_WAIT_V(2); PG8_BAR;
.Lhq_done:
	s_mov_b64 exec, -1
	s_waitcnt vmcnt(0) lgkmcnt(0)
	v_mov_b32_e32 v3, v193
	v_mov_b32_e32 v33, v194
	v_mov_b32_e32 v59, v195
	v_mov_b32_e32 v63, v196
	v_mov_b32_e32 v110, v197
	v_mov_b32_e32 v111, v198
	v_mov_b32_e32 v114, v199
	v_mov_b32_e32 v115, v200
	v_mov_b32_e32 v149, v201
	v_mov_b32_e32 v153, v202
	v_mov_b32_e32 v157, v203
	v_mov_b32_e32 v161, v204
	v_mov_b32_e32 v165, v205
	v_mov_b32_e32 v169, v206
	v_mov_b32_e32 v173, v207
	v_mov_b32_e32 v177, v208
	v_mov_b32_e32 v178, v209
	v_mov_b32_e32 v179, v210
	v_mov_b32_e32 v180, v211
	v_mov_b32_e32 v181, v212
	v_mov_b32_e32 v182, v214
	v_mov_b32_e32 v183, v215
	v_mov_b32_e32 v184, v216
	v_mov_b32_e32 v185, v218
	v_readlane_b32 s16, v251, 0
	v_readlane_b32 s17, v251, 1
	v_readlane_b32 s18, v251, 2
	v_readlane_b32 s19, v251, 3
	v_readlane_b32 s20, v251, 4
	v_readlane_b32 s21, v251, 5
	v_readlane_b32 s23, v251, 6
	v_readlane_b32 s25, v251, 7
	v_readlane_b32 s26, v251, 8
	v_readlane_b32 s33, v251, 9
	v_readlane_b32 s38, v251, 10
	v_readlane_b32 s39, v251, 11
	v_readlane_b32 s41, v251, 12
	v_readlane_b32 s42, v251, 13
	v_readlane_b32 s45, v251, 14
	v_readlane_b32 s48, v251, 15
	v_readlane_b32 s49, v251, 16
	v_readlane_b32 s50, v251, 17
	v_readlane_b32 s51, v251, 18
	v_readlane_b32 s74, v251, 19
	v_readlane_b32 s76, v251, 20
	s_nop 4
	s_branch .LBB0_295
.Lpq_skip:
	s_cbranch_vccnz .LBB0_295
	v_ashrrev_i32_e32 v3, 31, v1
	v_lshrrev_b32_e32 v3, 26, v3
	v_lshlrev_b32_e32 v2, 4, v1
	v_add_u32_e32 v3, v1, v3
	v_bfe_i32 v1, v1, 27, 1
	v_lshrrev_b32_e32 v1, 22, v1
	s_load_dwordx2 s[4:5], s[0:1], 0xa0
	v_add_u32_e32 v1, v2, v1
	v_and_b32_e32 v1, 0xfffffc00, v1
	v_sub_u32_e32 v1, v2, v1
	v_lshrrev_b32_e32 v4, 4, v1
	v_readlane_b32 s0, v255, 17
	v_bitop3_b32 v1, v4, v1, 32 bitop3:0x6c
	v_readlane_b32 s1, v255, 18
	s_waitcnt lgkmcnt(0)
	s_add_u32 s36, s4, 0x20600000
	v_ashrrev_i32_e32 v5, 31, v1
	s_mul_i32 s0, s0, 0x1780000
	s_addc_u32 s1, s5, 0
	v_ashrrev_i32_e32 v3, 6, v3
	v_lshrrev_b32_e32 v5, 26, v5
	s_add_u32 s0, s4, s0
	v_lshlrev_b32_e32 v4, 3, v3
	v_add_u32_e32 v5, v1, v5
	s_addc_u32 s2, s5, 0
	v_and_b32_e32 v4, -16, v4
	v_ashrrev_i32_e32 v6, 6, v5
	v_and_b32_e32 v5, 0xc0, v5
	s_add_u32 s8, s0, 0xc00000
	v_add_u32_e32 v4, v6, v4
	v_sub_u32_e32 v1, v1, v5
	s_addc_u32 s0, s2, 0
	v_lshlrev_b32_e32 v3, 5, v3
	v_ashrrev_i16_sdwa v1, v188, sext(v1) dst_sel:DWORD dst_unused:UNUSED_PAD src0_sel:DWORD src1_sel:BYTE_0
	v_lshlrev_b32_e32 v5, 1, v4
	v_lshrrev_b32_e32 v7, 2, v4
	v_and_b32_e32 v6, 3, v6
	s_mov_b32 s2, 0x1fffe0
	v_and_b32_e32 v3, 32, v3
	v_bfe_i32 v1, v1, 0, 16
	v_and_b32_e32 v5, 24, v5
	v_and_b32_e32 v7, 4, v7
	v_and_or_b32 v6, v4, s2, v6
	v_or3_b32 v5, v6, v7, v5
	v_add_lshl_u32 v1, v3, v1, 1
	v_lshl_add_u32 v193, v4, 11, v1
	v_lshl_add_u32 v194, v5, 11, v1
	v_add_u32_e32 v1, 0x2000, v2
	v_ashrrev_i32_e32 v2, 31, v1
	v_lshrrev_b32_e32 v2, 22, v2
	v_add_u32_e32 v2, v1, v2
	v_ashrrev_i32_e32 v2, 10, v2
	v_mul_i32_i24_e32 v3, 0x400, v2
	v_sub_u32_e32 v1, v1, v3
	v_lshrrev_b32_e32 v3, 4, v1
	v_bitop3_b32 v1, v3, v1, 32 bitop3:0x6c
	v_ashrrev_i32_e32 v4, 31, v1
	v_lshrrev_b32_e32 v4, 26, v4
	v_lshlrev_b32_e32 v3, 3, v2
	v_add_u32_e32 v4, v1, v4
	v_and_b32_e32 v3, -16, v3
	v_ashrrev_i32_e32 v5, 6, v4
	v_and_b32_e32 v4, 0xc0, v4
	s_ashr_i32 s17, s16, 6
	v_add_u32_e32 v3, v5, v3
	v_sub_u32_e32 v1, v1, v4
	v_lshlrev_b32_e32 v2, 5, v2
	v_ashrrev_i16_sdwa v1, v188, sext(v1) dst_sel:DWORD dst_unused:UNUSED_PAD src0_sel:DWORD src1_sel:BYTE_0
	v_lshlrev_b32_e32 v4, 1, v3
	v_lshrrev_b32_e32 v6, 2, v3
	v_and_b32_e32 v5, 3, v5
	s_and_b32 s9, s0, 0xffff
	s_lshl_b32 s0, s17, 10
	v_and_b32_e32 v2, 32, v2
	v_bfe_i32 v1, v1, 0, 16
	v_and_b32_e32 v4, 24, v4
	v_and_b32_e32 v6, 4, v6
	v_and_or_b32 v5, v3, s2, v5
	s_add_i32 s22, s0, 0
	v_or3_b32 v4, v5, v6, v4
	v_add_lshl_u32 v1, v2, v1, 1
	s_add_i32 s23, s22, 0x10000
	v_lshl_add_u32 v195, v3, 11, v1
	v_lshl_add_u32 v196, v4, 11, v1
	s_mov_b32 s10, s38
	s_mov_b32 s11, s39
	v_mov_b32_e32 v1, 0x7f7f7f7f
	s_mov_b32 m0, s23
	v_readlane_b32 s0, v253, 46
	s_add_i32 s24, s22, 0x12000
	s_add_i32 s25, s22, 0x14000
	s_add_i32 s26, s22, 0x16000
	s_and_b32 s37, s1, 0xffff
	s_nop 0
	buffer_load_dwordx4 v194, s[8:11], s0 offen lds
	s_mov_b32 m0, s24
	s_add_i32 s27, s22, 0x2000
	buffer_load_dwordx4 v196, s[8:11], s0 offen lds
	s_mov_b32 m0, s25
	v_readlane_b32 s0, v253, 40
	s_add_i32 s28, s22, 0x4000
	s_add_i32 s29, s22, 0x6000
	s_ashr_i32 s18, s16, 8
	s_cmp_eq_u32 s18, 1
	s_nop 0
	buffer_load_dwordx4 v194, s[8:11], s0 offen lds
	s_mov_b32 m0, s26
	s_nop 0
	buffer_load_dwordx4 v196, s[8:11], s0 offen lds
	s_mov_b32 m0, s22
	v_readlane_b32 s0, v253, 44
	s_nop 4
	buffer_load_dwordx4 v193, s[36:39], s0 offen lds
	s_mov_b32 m0, s27
	s_nop 0
	buffer_load_dwordx4 v195, s[36:39], s0 offen lds
	s_mov_b32 m0, s28
	v_readlane_b32 s0, v253, 42
	s_nop 4
	buffer_load_dwordx4 v193, s[36:39], s0 offen lds
	s_mov_b32 m0, s29
	s_nop 0
	buffer_load_dwordx4 v195, s[36:39], s0 offen lds
	s_cselect_b64 s[0:1], -1, 0
	s_cmp_lg_u32 s18, 1
	s_cbranch_scc1 .LBB0_268
	s_barrier

;     __device__ __forceinline__ bool next(int i, Unit& u) const { u.e = 0; u.ti = 0; return grid_order<WGM, ROT>(nM, nN, G, c, i, u.pm, u.pn); }
;     __device__ __forceinline__ bool next(int i, Unit& u) const { u.e = i & 1; u.ti = 0; return grid_order<WGM_MIX, ROT_MIX>(nM, nN, G, c, i >> 1, u.pm, u.pn); }
;     const int nwg = nM * nN; const long L = (long)i * G + c; if (L >= nwg) return false;
;     int wgid = (int)L; const int xcd = wgid % NXCD; { const int q = nwg / NXCD, r = nwg % NXCD, off = wgid / NXCD; wgid = (xcd < r ? xcd * (q + 1) : r * (q + 1) + (xcd - r) * q) + off; }
;     const int nig = WGM * nN, gid = wgid / nig, fm = gid * WGM, gsz = (nM - fm) < WGM ? (nM - fm) : WGM;
;     pm = fm + ((wgid % nig) % gsz); pn = (wgid % nig) / gsz;
;     if (ROT != 0 && (nwg % NXCD) == 0 && ((nwg / NXCD) % nig) == 0) pn = (pn + ROT * xcd) % nN;
;     return true;
; template <class Epi, class Sched, class AMap, bool ALIGN_EPI, bool F8 = false, bool SEG2 = false>
; __device__ __forceinline__ void gemm_phase(LAS unsigned char* lds, const int tid, const bf16_t* A, const bf16_t* Bt, size_t bstride, int K, const Sched& S, const AMap& AM, const Epi& E) {
;     ...
;         if constexpr (!AMap::GATHER) has_next = S.next(ui + 1, nxt);
.LBB0_271:
	s_add_i32 s43, s43, 1
	s_mul_i32 s4, s43, s75
	s_mul_hi_u32 s5, s43, s100
	s_add_i32 s5, s5, s4
	s_mul_i32 s4, s43, s100
	v_readlane_b32 s10, v253, 4
	s_add_u32 s10, s4, s10
	v_readlane_b32 s4, v253, 33
	s_addc_u32 s11, s5, s4
	v_mov_b64_e32 v[0:1], 0xbc0
	v_cmp_lt_i64_e64 s[4:5], s[10:11], v[0:1]
	v_mov_b64_e32 v[0:1], 0xbbf
	v_cmp_gt_i64_e32 vcc, s[10:11], v[0:1]
	s_cbranch_vccnz .LBB0_273
	s_ashr_i32 s11, s10, 31
	s_lshr_b32 s11, s11, 29
	s_add_i32 s11, s10, s11
	s_ashr_i32 s20, s11, 3
	s_and_b32 s11, s11, -8
	s_sub_i32 s10, s10, s11
	s_cmp_lt_i32 s10, 0
	s_cselect_b32 s11, s66, 0x178
	s_mul_i32 s11, s10, s11
	s_add_i32 s11, s11, s20
	s_mul_hi_i32 s20, s11, 0xae4c415d
	s_add_i32 s20, s20, s11
	s_lshr_b32 s21, s20, 31
	s_ashr_i32 s20, s20, 7
	s_add_i32 s20, s20, s21
	s_lshl_b32 s21, s20, 2
	s_sub_i32 s45, 64, s21
	s_min_i32 s45, s45, 4
	s_abs_i32 s46, s45
	v_cvt_f32_u32_e32 v0, s46
	s_sub_i32 s50, 0, s46
	s_mulk_i32 s20, 0xbc
	s_sub_i32 s11, s11, s20
	v_rcp_iflag_f32_e32 v0, v0
	s_abs_i32 s20, s11
	s_xor_b32 s47, s11, s45
	s_ashr_i32 s47, s47, 31
	v_mul_f32_e32 v0, 0x4f7ffffe, v0
	v_cvt_u32_f32_e32 v0, v0
	s_mul_i32 s10, s10, 6
	v_readfirstlane_b32 s55, v0
	s_mul_i32 s50, s50, s55
	s_mul_hi_u32 s50, s55, s50
	s_add_i32 s55, s55, s50
	s_mul_hi_u32 s50, s20, s55
	s_mul_i32 s55, s50, s46
	s_sub_i32 s20, s20, s55
	s_add_i32 s56, s50, 1
	s_sub_i32 s55, s20, s46
	s_cmp_ge_u32 s20, s46
	s_cselect_b32 s50, s56, s50
	s_cselect_b32 s20, s55, s20
	s_add_i32 s55, s50, 1
	s_cmp_ge_u32 s20, s46
	s_cselect_b32 s20, s55, s50
	s_xor_b32 s20, s20, s47
	s_sub_i32 s20, s20, s47
	s_mul_i32 s45, s20, s45
	s_sub_i32 s11, s11, s45
	s_add_i32 s10, s20, s10
	s_add_i32 s45, s21, s11
	s_mul_i32 s11, s10, 0xffffae4d
	s_lshr_b32 s11, s11, 16
	s_add_i32 s11, s11, s10
	s_sext_i32_i16 s20, s11
	s_ashr_i32 s20, s20, 5
	s_bfe_u32 s11, s11, 0x1000f
	s_add_i32 s11, s20, s11
	s_mul_i32 s11, s11, 47
	s_sub_i32 s10, s10, s11
	s_sext_i32_i16 s46, s10

; #define LAS __attribute__((address_space(3)))
;     ...
;         LAS float* scr = (LAS float*)(lds + wave * 16640);
;         const int gw = vcu * NWAVES + wave, NGW = G * NWAVES;
;         constexpr int C_IN = 32 * 188, C_OA = 8 * 32, C_OB = 16 * 32, C_O = 32 * 32, C_GU = 16 * 32 * 32, C_DN = 16 * 16 * 32, C_L = C_IN + C_OA + C_OB + C_O + C_GU + C_DN, NIT = DEPTH * C_L;
;         const int q4 = lane & 15, kk = lane >> 4;
;     ...
;         int it = gw; TrDesc dA, dB; f32x4 vA[16], vB[16];
;         if (it < NIT) { dA = decode(NIT - 1 - it); tr_load(dA, vA); }
.Lhp_entry:
	v_writelane_b32 v251, s16, 0
	v_writelane_b32 v251, s17, 1
	v_writelane_b32 v251, s18, 2
	v_writelane_b32 v251, s19, 3
	v_writelane_b32 v251, s20, 4
	v_writelane_b32 v251, s21, 5
	v_writelane_b32 v251, s23, 6
	v_writelane_b32 v251, s25, 7
	v_writelane_b32 v251, s26, 8
	v_writelane_b32 v251, s33, 9
	v_writelane_b32 v251, s38, 10
	v_writelane_b32 v251, s39, 11
	v_writelane_b32 v251, s41, 12
	v_writelane_b32 v251, s42, 13
	v_writelane_b32 v251, s45, 14
	v_writelane_b32 v251, s48, 15
	v_writelane_b32 v251, s49, 16
	v_writelane_b32 v251, s50, 17
	v_writelane_b32 v251, s51, 18
	v_writelane_b32 v251, s74, 19
	v_writelane_b32 v251, s76, 20
	v_mov_b32_e32 v193, v3
	v_mov_b32_e32 v194, v33
	v_mov_b32_e32 v195, v59
	v_mov_b32_e32 v196, v63
	v_mov_b32_e32 v197, v110
	v_mov_b32_e32 v198, v111
	v_mov_b32_e32 v199, v114
	v_mov_b32_e32 v200, v115
	v_mov_b32_e32 v201, v149
	v_mov_b32_e32 v202, v153
	v_mov_b32_e32 v203, v157
	v_mov_b32_e32 v204, v161
	v_mov_b32_e32 v205, v165
	v_mov_b32_e32 v206, v169
	v_mov_b32_e32 v207, v173
	v_mov_b32_e32 v208, v177
	v_mov_b32_e32 v209, v178
	v_mov_b32_e32 v210, v179
	v_mov_b32_e32 v211, v180
	v_mov_b32_e32 v212, v181
	v_mov_b32_e32 v214, v182
	v_mov_b32_e32 v215, v183
	v_mov_b32_e32 v216, v184
	v_mov_b32_e32 v218, v185
	v_readlane_b32 s76, v253, 4
	v_readlane_b32 s8, v253, 0
	v_readlane_b32 s9, v253, 1
	s_nop 1
	s_and_b32 s0, s76, 7
	s_lshr_b32 s1, s76, 3
	s_sub_i32 s1, s1, 24
	s_lshl_b32 s0, s0, 2
	s_lshr_b32 s2, s1, 1
	s_add_i32 s0, s0, s2
	s_and_b32 s1, s1, 1
	s_lshr_b32 s2, s0, 2
	s_lshl_b32 s2, s2, 3
	s_lshl_b32 s1, s1, 2
	s_and_b32 s0, s0, 3
	s_or_b32 s2, s2, s1
	s_or_b32 s76, s2, s0
	s_lshr_b32 s33, s78, 6
	s_movk_i32 s74, 64
	s_load_dwordx2 s[10:11], s[8:9], 0xa0
	v_mbcnt_lo_u32_b32 v69, -1, 0
	v_mbcnt_hi_u32_b32 v69, -1, v69
	s_mov_b64 exec, -1
	v_lshlrev_b32_e32 v76, 3, v69
	s_waitcnt lgkmcnt(0)
	s_lshl_b32 s47, s76, 3
	s_add_i32 s47, s47, s33
	s_add_i32 s47, s47, s100
	v_and_b32_e32 v2, 15, v69
	s_cmp_ge_i32 s47, s101
	v_ashrrev_i32_e32 v133, 4, v69
	s_cbranch_scc1 .LBB0_36_hp
	s_sub_i32 s1, 0xfcff, s47
	s_mul_hi_u32 s0, s1, 0x81848da9
	s_lshr_b32 s0, s0, 14
	s_mul_i32 s2, s0, 0x7e80
	s_sub_i32 s17, s1, s2
	s_cmpk_gt_u32 s17, 0x177f
	s_cbranch_scc0 .LBB0_37_hp
	s_cmpk_gt_u32 s17, 0x187f
	s_cbranch_scc0 .LBB0_39_hp
	s_cmpk_gt_u32 s17, 0x1a7f
	s_cbranch_scc0 .LBB0_40_hp
	s_cmpk_gt_u32 s17, 0x1e7f
	s_cbranch_scc0 .LBB0_41_hp
	s_lshl_b32 s1, s17, 6
	s_cmpk_gt_u32 s17, 0x5e7f
	s_cbranch_scc0 .LBB0_42_hp
	s_add_i32 s2, s17, 0xffffa180
	s_lshr_b32 s4, s2, 9
	s_lshl_b32 s2, s2, 1
	s_and_b32 s18, s2, 0x3c0
	s_load_dwordx2 s[2:3], s[8:9], 0x88
	s_lshl_b32 s5, s0, 4
	s_add_i32 s6, s4, s5
	s_mov_b32 s7, 0
	s_and_b32 s16, s1, 0x7c0
	s_lshl_b64 s[4:5], s[6:7], 23
	s_waitcnt lgkmcnt(0)
	s_add_u32 s4, s2, s4
	s_addc_u32 s5, s3, s5
	s_lshl_b64 s[2:3], s[6:7], 21
	s_add_u32 s2, s10, s2
	s_addc_u32 s3, s11, s3
	s_add_u32 s6, s2, 0x18600000
	v_lshl_or_b32 v0, v2, 2, s16
	s_addc_u32 s7, s3, 0
	s_mov_b64 s[2:3], 0
	s_branch .LBB0_43_hp
